# down GEMM: the NEXT unit's slot-list entries are requested during the current epilogue (one unit ahead, after the current ones are copied out), first unit's in the phase prologue; removes the load lat
# baseline (speedup 1.0000x reference)
; #define PG8_STAGE(bufoff, gbase, voff) do { _Pragma("unroll") for (int _i = 0; _i < 2; ++_i) \
;         __builtin_amdgcn_global_load_lds((const unsigned*)((const char*)(gbase) + (voff)[_i]), (PG8_LAS unsigned*)(lds + (bufoff) + ldsw + _i * 8192), 16, 0, 0); } while (0)
; #define PG8_WAIT_V(n) asm volatile("s_waitcnt vmcnt(" #n ")" ::: "memory")
; #define PG8_BAR __builtin_amdgcn_s_barrier()
;     __device__ __forceinline__ void operator()(const f32x4 (&acc)[2][2][4][2], const Unit& u, int wr, int wc, int fr, int fq) const {
;     ...
;         for (int ai = 0; ai < 2; ++ai)
; #pragma unroll
;             for (int m = 0; m < 4; ++m) { const int rl = rl0 + ai * HALF + m * 16;
;                 sr[ai][m] = SLOT[(size_t)u.aux * GCAP_SLOTS + (size_t)u.lt * BM + (rl < u.rows ? rl : 0)]; }
; template <class Epi, class Sched, bool ALIGN_EPI = false, bool SP2 = false, bool GATHER = false>
; __device__ __forceinline__ void gemm_phase(PG8_LAS unsigned char* lds, const Gemm g, const Sched& S, const Epi& E, const int2* gslot = nullptr, PG8_LAS unsigned char* gtab = nullptr) {
;     ...
;         PG8_STAGE(PG8_SB(1, 0), cB + kstep, voffB); PG8_STAGE(PG8_SA(1, 0), cA + kstep, PG8_VA(vC, 0)); PG8_STAGE(PG8_SB(1, 1), cB + hstep + kstep, voffB);
;         PG8_WAIT_V(6); PG8_BAR;
.LBB0_1164:
	s_add_u32 s22, s8, 0x92000000
	s_addc_u32 s23, s9, 0
	s_add_u32 s53, s8, 0xa2400000
	s_addc_u32 s56, s9, 0
	s_add_i32 m0, s47, 0x18000
	v_lshl_add_u64 v[24:25], v[24:25], 0, s[54:55]
	s_lshl_b32 s2, s15, 13
	s_lshl_b32 s5, s14, 7
	s_waitcnt vmcnt(2)
	s_barrier
	global_load_lds_dwordx4 v[24:25], off
	v_lshl_add_u64 v[22:23], v[22:23], 0, s[54:55]
	s_add_i32 m0, s47, 0x1a000
	s_add_i32 s58, s47, 0x8000
	s_add_i32 s59, s47, 0xa000
	global_load_lds_dwordx4 v[22:23], off
	v_lshl_add_u64 v[18:19], v[18:19], 0, s[54:55]
	s_mov_b32 m0, s58
	s_add_u32 s8, s10, 0x40080
	global_load_lds_dwordx4 v[18:19], off
	v_lshl_add_u64 v[18:19], v[20:21], 0, s[54:55]
	s_mov_b32 m0, s59
	s_addc_u32 s9, s11, 0
	global_load_lds_dwordx4 v[18:19], off
	s_add_i32 m0, s47, 0x1c000
	v_lshl_add_u64 v[18:19], s[8:9], 0, v[0:1]
	global_load_lds_dwordx4 v[18:19], off
	v_lshl_add_u64 v[18:19], s[8:9], 0, v[146:147]
	s_add_i32 m0, s47, 0x1e000
	s_cmpk_lt_u32 s7, 0x100
	global_load_lds_dwordx4 v[18:19], off
	v_and_b32_e32 v18, 15, v26
	v_lshlrev_b32_e32 v19, 1, v28
	v_lshl_or_b32 v167, s15, 6, v18
	v_lshl_or_b32 v18, v18, 6, v19
	v_lshlrev_b32_e32 v19, 2, v26
	v_and_b32_e32 v19, 32, v19
	v_bitop3_b32 v20, v18, s2, v19 bitop3:0xde
	v_bitop3_b32 v168, v18, s5, v19 bitop3:0xde
	v_lshlrev_b32_e32 v18, 14, v32
	v_and_b32_e32 v18, 0xffff8000, v18
	v_lshl_add_u32 v18, v31, 11, v18
	v_and_b32_e32 v19, 1, v32
	v_lshl_or_b32 v18, v19, 6, v18
	v_lshl_add_u32 v152, v33, 1, v18
	v_lshlrev_b32_e32 v18, 14, v27
	v_and_b32_e32 v18, 0xffff8000, v18
	s_waitcnt vmcnt(6)
	v_lshl_add_u32 v18, v29, 11, v18
	v_and_b32_e32 v19, 1, v27
	v_lshl_or_b32 v18, v19, 6, v18
	s_cselect_b64 s[24:25], -1, 0
	v_or_b32_e32 v169, s14, v28
	v_mov_b32_e32 v153, v1
	v_lshl_add_u32 v154, v30, 1, v18
	v_mov_b32_e32 v155, v1
	s_mov_b32 s60, 0
	v_add_u32_e32 v170, 0, v20
	v_readlane_b32 s66, v253, 50
	s_barrier
	s_and_b32 s68, s4, 31
	s_and_b32 s69, s6, 0x7f
	s_lshl_b32 s68, s68, 18
	s_lshl_b32 s69, s69, 11
	s_add_i32 s68, s68, s69
	s_add_u32 s68, s53, s68
	s_addc_u32 s69, s56, 0
	v_mov_b32_e32 v220, v167
	v_subrev_u32_e32 v221, s65, v220
	v_ashrrev_i32_e32 v221, 31, v221
	v_and_b32_e32 v220, v221, v220
	v_mov_b32_e32 v221, 0
	v_lshl_add_u64 v[220:221], v[220:221], 3, s[68:69]
	global_load_dwordx2 v[220:221], v[220:221], off
	v_add_u32_e32 v222, 0x10, v167
	v_subrev_u32_e32 v223, s65, v222
	v_ashrrev_i32_e32 v223, 31, v223
	v_and_b32_e32 v222, v223, v222
	v_mov_b32_e32 v223, 0
	v_lshl_add_u64 v[222:223], v[222:223], 3, s[68:69]
	global_load_dwordx2 v[222:223], v[222:223], off
	v_add_u32_e32 v224, 0x20, v167
	v_subrev_u32_e32 v225, s65, v224
	v_ashrrev_i32_e32 v225, 31, v225
	v_and_b32_e32 v224, v225, v224
	v_mov_b32_e32 v225, 0
	v_lshl_add_u64 v[224:225], v[224:225], 3, s[68:69]
	global_load_dwordx2 v[224:225], v[224:225], off
	v_add_u32_e32 v226, 0x30, v167
	v_subrev_u32_e32 v227, s65, v226
	v_ashrrev_i32_e32 v227, 31, v227
	v_and_b32_e32 v226, v227, v226
	v_mov_b32_e32 v227, 0
	v_lshl_add_u64 v[226:227], v[226:227], 3, s[68:69]
	global_load_dwordx2 v[226:227], v[226:227], off
	v_add_u32_e32 v240, 0x80, v167
	v_subrev_u32_e32 v241, s65, v240
	v_ashrrev_i32_e32 v241, 31, v241
	v_and_b32_e32 v240, v241, v240
	v_mov_b32_e32 v241, 0
	v_lshl_add_u64 v[240:241], v[240:241], 3, s[68:69]
	global_load_dwordx2 v[240:241], v[240:241], off
	v_add_u32_e32 v242, 0x90, v167
	v_subrev_u32_e32 v243, s65, v242
	v_ashrrev_i32_e32 v243, 31, v243
	v_and_b32_e32 v242, v243, v242
	v_mov_b32_e32 v243, 0
	v_lshl_add_u64 v[242:243], v[242:243], 3, s[68:69]
	global_load_dwordx2 v[242:243], v[242:243], off
	v_add_u32_e32 v244, 0xa0, v167
	v_subrev_u32_e32 v245, s65, v244
	v_ashrrev_i32_e32 v245, 31, v245
	v_and_b32_e32 v244, v245, v244
	v_mov_b32_e32 v245, 0
	v_lshl_add_u64 v[244:245], v[244:245], 3, s[68:69]
	global_load_dwordx2 v[244:245], v[244:245], off
	v_add_u32_e32 v246, 0xb0, v167
	v_subrev_u32_e32 v247, s65, v246
	v_ashrrev_i32_e32 v247, 31, v247
	v_and_b32_e32 v246, v247, v246
	v_mov_b32_e32 v247, 0
	v_lshl_add_u64 v[246:247], v[246:247], 3, s[68:69]
	global_load_dwordx2 v[246:247], v[246:247], off
	s_branch .LBB0_1167

; __device__ __forceinline__ u32x4 pack8(const f32x4 v0, const f32x4 v1) { u32x4 w; w.x = cvt_pk_bf16(v0[0], v0[1]); w.y = cvt_pk_bf16(v0[2], v0[3]); w.z = cvt_pk_bf16(v1[0], v1[1]); w.w = cvt_pk_bf16(v1[2], v1[3]); return w; }
;     __device__ __forceinline__ void operator()(const f32x4 (&acc)[2][2][4][2], const Unit& u, int wr, int wc, int fr, int fq) const {
;         int rl0 = wr * 64 + fr; asm volatile("" : "+v"(rl0));
;         const int col0 = u.pn * BM + wc * 32 + 8 * fq;
;         int2 sr[2][4];
; #pragma unroll
;         for (int ai = 0; ai < 2; ++ai)
; #pragma unroll
;             for (int m = 0; m < 4; ++m) { const int rl = rl0 + ai * HALF + m * 16;
;                 sr[ai][m] = SLOT[(size_t)u.aux * GCAP_SLOTS + (size_t)u.lt * BM + (rl < u.rows ? rl : 0)]; }
;         __builtin_amdgcn_sched_barrier(0);
; #pragma unroll
;         for (int ai = 0; ai < 2; ++ai)
; #pragma unroll
;             for (int m = 0; m < 4; ++m) { const int rl = rl0 + ai * HALF + m * 16; const bool ok = rl < u.rows;
;                 const int2 s = sr[ai][m]; const float w = __int_as_float(s.y); bf16_t* rowp = YE + (size_t)(ok ? s.x : dummy_row) * 1024 + col0;
; #pragma unroll
;                 for (int bj = 0; bj < 2; ++bj) *(u32x4*)(rowp + bj * HALF) = pack8(acc[ai][bj][m][0] * w, acc[ai][bj][m][1] * w); }
.LBB0_1177:
	s_ashr_i32 s9, s8, 31
	s_lshl_b64 s[8:9], s[8:9], 12
	s_add_u32 s2, s43, s8
	s_addc_u32 s7, s44, s9
	s_lshl_b32 s8, s5, 8
	s_ashr_i32 s9, s8, 31
	s_lshl_b64 s[8:9], s[8:9], 2
	s_add_u32 s2, s2, s8
	s_addc_u32 s5, s7, s9
	s_add_u32 s8, s2, s46
	s_addc_u32 s9, s5, 0
	global_load_dwordx4 v[70:73], v166, s[8:9] offset:16
	global_load_dwordx4 v[78:81], v166, s[8:9]
	global_load_dwordx4 v[66:69], v166, s[8:9] offset:528
	global_load_dwordx4 v[74:77], v166, s[8:9] offset:512
	s_ashr_i32 s5, s4, 31
	v_mov_b32_e32 v164, v167
	s_ashr_i32 s7, s6, 31
	s_lshl_b64 s[4:5], s[4:5], 18
	s_add_u32 s2, s53, s4
	v_add_u32_e32 v160, 32, v164
	s_addc_u32 s8, s56, s5
	s_lshl_b64 s[4:5], s[6:7], 11
	v_cmp_gt_i32_e64 s[18:19], s65, v164
	v_add_u32_e32 v158, 16, v164
	v_cmp_gt_i32_e64 s[12:13], s65, v160
	v_add_u32_e32 v162, 48, v164
	s_add_u32 s68, s2, s4
	v_cndmask_b32_e64 v156, 0, v164, s[18:19]
	v_cmp_gt_i32_e64 s[14:15], s65, v158
	v_cndmask_b32_e64 v160, 0, v160, s[12:13]
	v_cmp_gt_i32_e64 s[10:11], s65, v162
	s_addc_u32 s69, s8, s5
	v_ashrrev_i32_e32 v157, 31, v156
	v_cndmask_b32_e64 v158, 0, v158, s[14:15]
	v_ashrrev_i32_e32 v161, 31, v160
	v_cndmask_b32_e64 v162, 0, v162, s[10:11]
	v_lshl_add_u64 v[156:157], v[156:157], 3, s[68:69]
	v_ashrrev_i32_e32 v159, 31, v158
	v_lshl_add_u64 v[160:161], v[160:161], 3, s[68:69]
	v_ashrrev_i32_e32 v163, 31, v162
	v_lshl_add_u64 v[158:159], v[158:159], 3, s[68:69]
	v_lshl_add_u64 v[162:163], v[162:163], 3, s[68:69]
	s_waitcnt vmcnt(12)
	v_mov_b64_e32 v[172:173], v[220:221]
	v_mov_b64_e32 v[174:175], v[222:223]
	v_mov_b64_e32 v[176:177], v[224:225]
	v_mov_b64_e32 v[178:179], v[226:227]
	v_add_u32_e32 v156, 0x80, v164
	v_add_u32_e32 v160, 0xa0, v164
	v_cmp_gt_i32_e64 s[8:9], s65, v156
	v_add_u32_e32 v158, 0x90, v164
	v_cmp_gt_i32_e64 s[4:5], s65, v160
	v_add_u32_e32 v162, 0xb0, v164
	v_cndmask_b32_e64 v156, 0, v156, s[8:9]
	v_cmp_gt_i32_e64 s[6:7], s65, v158
	v_cndmask_b32_e64 v160, 0, v160, s[4:5]
	v_cmp_gt_i32_e32 vcc, s65, v162
	v_ashrrev_i32_e32 v157, 31, v156
	v_cndmask_b32_e64 v158, 0, v158, s[6:7]
	v_ashrrev_i32_e32 v161, 31, v160
	v_cndmask_b32_e32 v162, 0, v162, vcc
	v_lshl_add_u64 v[156:157], v[156:157], 3, s[68:69]
	v_ashrrev_i32_e32 v159, 31, v158
	v_lshl_add_u64 v[160:161], v[160:161], 3, s[68:69]
	v_ashrrev_i32_e32 v163, 31, v162
	v_lshl_add_u64 v[158:159], v[158:159], 3, s[68:69]
	v_lshl_add_u64 v[180:181], v[162:163], 3, s[68:69]
	v_mov_b64_e32 v[164:165], v[240:241]
	v_mov_b64_e32 v[162:163], v[242:243]
	s_nop 0
	v_mov_b64_e32 v[160:161], v[244:245]
	s_nop 0
	v_mov_b64_e32 v[156:157], v[246:247]
	s_and_b32 s68, s63, 31
	s_and_b32 s69, s62, 0x7f
	s_lshl_b32 s68, s68, 18
	s_lshl_b32 s69, s69, 11
	s_add_i32 s68, s68, s69
	s_add_u32 s68, s53, s68
	s_addc_u32 s69, s56, 0
	v_mov_b32_e32 v220, v167
	v_subrev_u32_e32 v221, s61, v220
	v_ashrrev_i32_e32 v221, 31, v221
	v_and_b32_e32 v220, v221, v220
	v_mov_b32_e32 v221, 0
	v_lshl_add_u64 v[220:221], v[220:221], 3, s[68:69]
	global_load_dwordx2 v[220:221], v[220:221], off
	v_add_u32_e32 v222, 0x10, v167
	v_subrev_u32_e32 v223, s61, v222
	v_ashrrev_i32_e32 v223, 31, v223
	v_and_b32_e32 v222, v223, v222
	v_mov_b32_e32 v223, 0
	v_lshl_add_u64 v[222:223], v[222:223], 3, s[68:69]
	global_load_dwordx2 v[222:223], v[222:223], off
	v_add_u32_e32 v224, 0x20, v167
	v_subrev_u32_e32 v225, s61, v224
	v_ashrrev_i32_e32 v225, 31, v225
	v_and_b32_e32 v224, v225, v224
	v_mov_b32_e32 v225, 0
	v_lshl_add_u64 v[224:225], v[224:225], 3, s[68:69]
	global_load_dwordx2 v[224:225], v[224:225], off
	v_add_u32_e32 v226, 0x30, v167
	v_subrev_u32_e32 v227, s61, v226
	v_ashrrev_i32_e32 v227, 31, v227
	v_and_b32_e32 v226, v227, v226
	v_mov_b32_e32 v227, 0
	v_lshl_add_u64 v[226:227], v[226:227], 3, s[68:69]
	global_load_dwordx2 v[226:227], v[226:227], off
	v_add_u32_e32 v240, 0x80, v167
	v_subrev_u32_e32 v241, s61, v240
	v_ashrrev_i32_e32 v241, 31, v241
	v_and_b32_e32 v240, v241, v240
	v_mov_b32_e32 v241, 0
	v_lshl_add_u64 v[240:241], v[240:241], 3, s[68:69]
	global_load_dwordx2 v[240:241], v[240:241], off
	v_add_u32_e32 v242, 0x90, v167
	v_subrev_u32_e32 v243, s61, v242
	v_ashrrev_i32_e32 v243, 31, v243
	v_and_b32_e32 v242, v243, v242
	v_mov_b32_e32 v243, 0
	v_lshl_add_u64 v[242:243], v[242:243], 3, s[68:69]
	global_load_dwordx2 v[242:243], v[242:243], off
	v_add_u32_e32 v244, 0xa0, v167
	v_subrev_u32_e32 v245, s61, v244
	v_ashrrev_i32_e32 v245, 31, v245
	v_and_b32_e32 v244, v245, v244
	v_mov_b32_e32 v245, 0
	v_lshl_add_u64 v[244:245], v[244:245], 3, s[68:69]
	global_load_dwordx2 v[244:245], v[244:245], off
	v_add_u32_e32 v246, 0xb0, v167
	v_subrev_u32_e32 v247, s61, v246
	v_ashrrev_i32_e32 v247, 31, v247
	v_and_b32_e32 v246, v247, v246
	v_mov_b32_e32 v247, 0
	v_lshl_add_u64 v[246:247], v[246:247], 3, s[68:69]
	global_load_dwordx2 v[246:247], v[246:247], off
	v_lshl_or_b32 v158, s66, 8, v169
	v_cndmask_b32_e64 v180, v250, v172, s[18:19]
	v_ashrrev_i32_e32 v181, 31, v180
	v_ashrrev_i32_e32 v159, 31, v158
	v_lshlrev_b64 v[180:181], 11, v[180:181]
	v_lshl_add_u64 v[180:181], s[22:23], 0, v[180:181]
	v_lshlrev_b64 v[158:159], 1, v[158:159]
	v_lshl_add_u64 v[180:181], v[180:181], 0, v[158:159]
	v_pk_mul_f32 v[144:145], v[144:145], v[172:173] op_sel:[0,1]
	v_pk_mul_f32 v[142:143], v[142:143], v[172:173] op_sel:[0,1]
	v_pk_mul_f32 v[182:183], v[140:141], v[172:173] op_sel:[0,1]
	v_pk_mul_f32 v[140:141], v[138:139], v[172:173] op_sel:[0,1]
	v_cvt_pk_bf16_f32 v138, v142, v143
	v_cvt_pk_bf16_f32 v139, v144, v145
	v_pk_mul_f32 v[134:135], v[134:135], v[172:173] op_sel:[0,1]
	v_cvt_pk_bf16_f32 v140, v140, v141
	v_cvt_pk_bf16_f32 v141, v182, v183
	global_store_dwordx4 v[180:181], v[138:141], off
; __device__ __forceinline__ u32x4 pack8(const f32x4 v0, const f32x4 v1) { u32x4 w; w.x = cvt_pk_bf16(v0[0], v0[1]); w.y = cvt_pk_bf16(v0[2], v0[3]); w.z = cvt_pk_bf16(v1[0], v1[1]); w.w = cvt_pk_bf16(v1[2], v1[3]); return w; }
;     __device__ __forceinline__ void operator()(const f32x4 (&acc)[2][2][4][2], const Unit& u, int wr, int wc, int fr, int fq) const {
;     ...
; #pragma unroll
;         for (int ai = 0; ai < 2; ++ai)
; #pragma unroll
;             for (int m = 0; m < 4; ++m) { const int rl = rl0 + ai * HALF + m * 16; const bool ok = rl < u.rows;
;                 const int2 s = sr[ai][m]; const float w = __int_as_float(s.y); bf16_t* rowp = YE + (size_t)(ok ? s.x : dummy_row) * 1024 + col0;
; #pragma unroll
;                 for (int bj = 0; bj < 2; ++bj) *(u32x4*)(rowp + bj * HALF) = pack8(acc[ai][bj][m][0] * w, acc[ai][bj][m][1] * w); }
	v_pk_mul_f32 v[136:137], v[136:137], v[172:173] op_sel:[0,1]
	v_pk_mul_f32 v[128:129], v[128:129], v[174:175] op_sel:[0,1]
	v_pk_mul_f32 v[138:139], v[132:133], v[172:173] op_sel:[0,1]
	v_pk_mul_f32 v[132:133], v[130:131], v[172:173] op_sel:[0,1]
	v_cvt_pk_bf16_f32 v130, v134, v135
	v_cvt_pk_bf16_f32 v131, v136, v137
	v_pk_mul_f32 v[126:127], v[126:127], v[174:175] op_sel:[0,1]
	v_cvt_pk_bf16_f32 v132, v132, v133
	v_cvt_pk_bf16_f32 v133, v138, v139
	global_store_dwordx4 v[180:181], v[130:133], off offset:256
	v_pk_mul_f32 v[118:119], v[118:119], v[174:175] op_sel:[0,1]
	v_pk_mul_f32 v[120:121], v[120:121], v[174:175] op_sel:[0,1]
	v_cndmask_b32_e64 v130, v250, v174, s[14:15]
	v_ashrrev_i32_e32 v131, 31, v130
	v_lshlrev_b64 v[130:131], 11, v[130:131]
	v_lshl_add_u64 v[130:131], s[22:23], 0, v[130:131]
	v_lshl_add_u64 v[130:131], v[130:131], 0, v[158:159]
	v_pk_mul_f32 v[132:133], v[124:125], v[174:175] op_sel:[0,1]
	v_pk_mul_f32 v[124:125], v[122:123], v[174:175] op_sel:[0,1]
	v_cvt_pk_bf16_f32 v122, v126, v127
	v_cvt_pk_bf16_f32 v123, v128, v129
	v_pk_mul_f32 v[112:113], v[112:113], v[176:177] op_sel:[0,1]
	v_cvt_pk_bf16_f32 v124, v124, v125
	v_cvt_pk_bf16_f32 v125, v132, v133
	global_store_dwordx4 v[130:131], v[122:125], off
	v_pk_mul_f32 v[110:111], v[110:111], v[176:177] op_sel:[0,1]
	v_pk_mul_f32 v[102:103], v[102:103], v[176:177] op_sel:[0,1]
	v_pk_mul_f32 v[122:123], v[116:117], v[174:175] op_sel:[0,1]
	v_pk_mul_f32 v[116:117], v[114:115], v[174:175] op_sel:[0,1]
	v_cvt_pk_bf16_f32 v114, v118, v119
	v_cvt_pk_bf16_f32 v115, v120, v121
	v_pk_mul_f32 v[104:105], v[104:105], v[176:177] op_sel:[0,1]
	v_cvt_pk_bf16_f32 v116, v116, v117
	v_cvt_pk_bf16_f32 v117, v122, v123
	global_store_dwordx4 v[130:131], v[114:117], off offset:256
	v_pk_mul_f32 v[96:97], v[96:97], v[178:179] op_sel:[0,1]
	v_pk_mul_f32 v[94:95], v[94:95], v[178:179] op_sel:[0,1]
	v_cndmask_b32_e64 v114, v250, v176, s[12:13]
	v_ashrrev_i32_e32 v115, 31, v114
	v_lshlrev_b64 v[114:115], 11, v[114:115]
	v_lshl_add_u64 v[114:115], s[22:23], 0, v[114:115]
	v_lshl_add_u64 v[114:115], v[114:115], 0, v[158:159]
	v_pk_mul_f32 v[116:117], v[108:109], v[176:177] op_sel:[0,1]
	v_pk_mul_f32 v[108:109], v[106:107], v[176:177] op_sel:[0,1]
	v_cvt_pk_bf16_f32 v106, v110, v111
	v_cvt_pk_bf16_f32 v107, v112, v113
	v_pk_mul_f32 v[86:87], v[86:87], v[178:179] op_sel:[0,1]
	v_cvt_pk_bf16_f32 v108, v108, v109
	v_cvt_pk_bf16_f32 v109, v116, v117
	global_store_dwordx4 v[114:115], v[106:109], off
	v_pk_mul_f32 v[88:89], v[88:89], v[178:179] op_sel:[0,1]
	v_pk_mul_f32 v[64:65], v[64:65], v[164:165] op_sel:[0,1]
	v_pk_mul_f32 v[106:107], v[100:101], v[176:177] op_sel:[0,1]
	v_pk_mul_f32 v[100:101], v[98:99], v[176:177] op_sel:[0,1]
	v_cvt_pk_bf16_f32 v98, v102, v103
	v_cvt_pk_bf16_f32 v99, v104, v105
	v_pk_mul_f32 v[62:63], v[62:63], v[164:165] op_sel:[0,1]
	v_cvt_pk_bf16_f32 v100, v100, v101
	v_cvt_pk_bf16_f32 v101, v106, v107
	global_store_dwordx4 v[114:115], v[98:101], off offset:256
	v_pk_mul_f32 v[54:55], v[54:55], v[164:165] op_sel:[0,1]
	v_pk_mul_f32 v[56:57], v[56:57], v[164:165] op_sel:[0,1]
	v_cndmask_b32_e64 v98, v250, v178, s[10:11]
	v_ashrrev_i32_e32 v99, 31, v98
	v_lshlrev_b64 v[98:99], 11, v[98:99]
	v_lshl_add_u64 v[98:99], s[22:23], 0, v[98:99]
	v_lshl_add_u64 v[98:99], v[98:99], 0, v[158:159]
	v_pk_mul_f32 v[100:101], v[92:93], v[178:179] op_sel:[0,1]
	v_pk_mul_f32 v[92:93], v[90:91], v[178:179] op_sel:[0,1]
	v_cvt_pk_bf16_f32 v90, v94, v95
	v_cvt_pk_bf16_f32 v91, v96, v97
	v_pk_mul_f32 v[48:49], v[48:49], v[162:163] op_sel:[0,1]
	v_cvt_pk_bf16_f32 v92, v92, v93
	v_cvt_pk_bf16_f32 v93, v100, v101
	global_store_dwordx4 v[98:99], v[90:93], off
	v_pk_mul_f32 v[46:47], v[46:47], v[162:163] op_sel:[0,1]
	v_pk_mul_f32 v[38:39], v[38:39], v[162:163] op_sel:[0,1]
	v_pk_mul_f32 v[90:91], v[84:85], v[178:179] op_sel:[0,1]
	v_pk_mul_f32 v[84:85], v[82:83], v[178:179] op_sel:[0,1]
	v_cvt_pk_bf16_f32 v82, v86, v87
	v_cvt_pk_bf16_f32 v83, v88, v89
	v_pk_mul_f32 v[40:41], v[40:41], v[162:163] op_sel:[0,1]
	v_cvt_pk_bf16_f32 v84, v84, v85
	v_cvt_pk_bf16_f32 v85, v90, v91
	global_store_dwordx4 v[98:99], v[82:85], off offset:256
	v_pk_mul_f32 v[32:33], v[32:33], v[160:161] op_sel:[0,1]
	v_pk_mul_f32 v[30:31], v[30:31], v[160:161] op_sel:[0,1]
	v_cndmask_b32_e64 v82, v250, v164, s[8:9]
	v_ashrrev_i32_e32 v83, 31, v82
	v_lshlrev_b64 v[82:83], 11, v[82:83]
	v_lshl_add_u64 v[82:83], s[22:23], 0, v[82:83]
	v_lshl_add_u64 v[82:83], v[82:83], 0, v[158:159]
	v_pk_mul_f32 v[84:85], v[60:61], v[164:165] op_sel:[0,1]
	v_pk_mul_f32 v[60:61], v[58:59], v[164:165] op_sel:[0,1]
	v_cvt_pk_bf16_f32 v58, v62, v63
	v_cvt_pk_bf16_f32 v59, v64, v65
	v_pk_mul_f32 v[22:23], v[22:23], v[160:161] op_sel:[0,1]
	v_cvt_pk_bf16_f32 v60, v60, v61
	v_cvt_pk_bf16_f32 v61, v84, v85
	s_waitcnt vmcnt(0)
; __device__ __forceinline__ u32x4 pack8(const f32x4 v0, const f32x4 v1) { u32x4 w; w.x = cvt_pk_bf16(v0[0], v0[1]); w.y = cvt_pk_bf16(v0[2], v0[3]); w.z = cvt_pk_bf16(v1[0], v1[1]); w.w = cvt_pk_bf16(v1[2], v1[3]); return w; }
; #define PG8_BAR __builtin_amdgcn_s_barrier()
;     __device__ __forceinline__ void operator()(const f32x4 (&acc)[2][2][4][2], const Unit& u, int wr, int wc, int fr, int fq) const {
;     ...
;         for (int ai = 0; ai < 2; ++ai)
; #pragma unroll
;             for (int m = 0; m < 4; ++m) { const int rl = rl0 + ai * HALF + m * 16; const bool ok = rl < u.rows;
;                 const int2 s = sr[ai][m]; const float w = __int_as_float(s.y); bf16_t* rowp = YE + (size_t)(ok ? s.x : dummy_row) * 1024 + col0;
; #pragma unroll
;                 for (int bj = 0; bj < 2; ++bj) *(u32x4*)(rowp + bj * HALF) = pack8(acc[ai][bj][m][0] * w, acc[ai][bj][m][1] * w); }
; template <class Epi, class Sched, bool ALIGN_EPI = false, bool SP2 = false, bool GATHER = false>
; __device__ __forceinline__ void gemm_phase(PG8_LAS unsigned char* lds, const Gemm g, const Sched& S, const Epi& E, const int2* gslot = nullptr, PG8_LAS unsigned char* gtab = nullptr) {
;     ...
;         if constexpr (!Epi::AFTER_DRAIN) { E(acc, cur, wr, wc, fr, fq); S.done(cur); }
;         if (!has_next) break;
;         E.init(acc, pre);
;         cur = nxt; cA = nA; cB = nB; ++ui;
;         if constexpr (GATHER) { _Pragma("unroll") for (int h_ = 0; h_ < 2; ++h_) _Pragma("unroll") for (int i_ = 0; i_ < 2; ++i_) vC[h_][i_] = vN[h_][i_]; }
;         if constexpr (ALIGN_EPI) { if (wr == 1) PG8_BAR; }
	global_store_dwordx4 v[82:83], v[58:61], off
	v_pk_mul_f32 v[24:25], v[24:25], v[160:161] op_sel:[0,1]
	v_pk_mul_f32 v[16:17], v[16:17], v[156:157] op_sel:[0,1]
	v_pk_mul_f32 v[58:59], v[52:53], v[164:165] op_sel:[0,1]
	v_pk_mul_f32 v[52:53], v[50:51], v[164:165] op_sel:[0,1]
	v_cvt_pk_bf16_f32 v50, v54, v55
	v_cvt_pk_bf16_f32 v51, v56, v57
	v_pk_mul_f32 v[14:15], v[14:15], v[156:157] op_sel:[0,1]
	v_cvt_pk_bf16_f32 v52, v52, v53
	v_cvt_pk_bf16_f32 v53, v58, v59
	global_store_dwordx4 v[82:83], v[50:53], off offset:256
	v_pk_mul_f32 v[8:9], v[8:9], v[156:157] op_sel:[0,1]
	v_pk_mul_f32 v[6:7], v[6:7], v[156:157] op_sel:[0,1]
	v_cndmask_b32_e64 v50, v250, v162, s[6:7]
	v_ashrrev_i32_e32 v51, 31, v50
	v_lshlrev_b64 v[50:51], 11, v[50:51]
	v_lshl_add_u64 v[50:51], s[22:23], 0, v[50:51]
	v_lshl_add_u64 v[50:51], v[50:51], 0, v[158:159]
	v_pk_mul_f32 v[52:53], v[44:45], v[162:163] op_sel:[0,1]
	v_pk_mul_f32 v[44:45], v[42:43], v[162:163] op_sel:[0,1]
	v_cvt_pk_bf16_f32 v42, v46, v47
	v_cvt_pk_bf16_f32 v43, v48, v49
	s_nop 0
	v_cvt_pk_bf16_f32 v44, v44, v45
	v_cvt_pk_bf16_f32 v45, v52, v53
	global_store_dwordx4 v[50:51], v[42:45], off
	s_nop 1
	v_pk_mul_f32 v[42:43], v[36:37], v[162:163] op_sel:[0,1]
	v_pk_mul_f32 v[36:37], v[34:35], v[162:163] op_sel:[0,1]
	v_cvt_pk_bf16_f32 v34, v38, v39
	v_cvt_pk_bf16_f32 v35, v40, v41
	s_nop 0
	v_cvt_pk_bf16_f32 v36, v36, v37
	v_cvt_pk_bf16_f32 v37, v42, v43
	global_store_dwordx4 v[50:51], v[34:37], off offset:256
	s_nop 1
	v_cndmask_b32_e64 v34, v250, v160, s[4:5]
	v_ashrrev_i32_e32 v35, 31, v34
	v_lshlrev_b64 v[34:35], 11, v[34:35]
	v_lshl_add_u64 v[34:35], s[22:23], 0, v[34:35]
	v_lshl_add_u64 v[34:35], v[34:35], 0, v[158:159]
	v_pk_mul_f32 v[36:37], v[28:29], v[160:161] op_sel:[0,1]
	v_pk_mul_f32 v[28:29], v[26:27], v[160:161] op_sel:[0,1]
	v_cvt_pk_bf16_f32 v26, v30, v31
	v_cvt_pk_bf16_f32 v27, v32, v33
	s_mov_b64 s[4:5], -1
	v_cvt_pk_bf16_f32 v28, v28, v29
	v_cvt_pk_bf16_f32 v29, v36, v37
	global_store_dwordx4 v[34:35], v[26:29], off
	s_nop 1
	v_pk_mul_f32 v[26:27], v[20:21], v[160:161] op_sel:[0,1]
	v_pk_mul_f32 v[20:21], v[18:19], v[160:161] op_sel:[0,1]
	v_cvt_pk_bf16_f32 v18, v22, v23
	v_cvt_pk_bf16_f32 v19, v24, v25
	s_nop 0
	v_cvt_pk_bf16_f32 v20, v20, v21
	v_cvt_pk_bf16_f32 v21, v26, v27
	global_store_dwordx4 v[34:35], v[18:21], off offset:256
	s_nop 1
	v_cndmask_b32_e32 v18, v250, v156, vcc
	v_ashrrev_i32_e32 v19, 31, v18
	v_lshlrev_b64 v[18:19], 11, v[18:19]
	v_lshl_add_u64 v[18:19], s[22:23], 0, v[18:19]
	v_lshl_add_u64 v[18:19], v[18:19], 0, v[158:159]
	v_pk_mul_f32 v[20:21], v[12:13], v[156:157] op_sel:[0,1]
	v_pk_mul_f32 v[12:13], v[10:11], v[156:157] op_sel:[0,1]
	v_cvt_pk_bf16_f32 v10, v14, v15
	v_cvt_pk_bf16_f32 v11, v16, v17
	s_andn2_b64 vcc, exec, s[30:31]
	v_cvt_pk_bf16_f32 v12, v12, v13
	v_cvt_pk_bf16_f32 v13, v20, v21
	global_store_dwordx4 v[18:19], v[10:13], off
	s_nop 1
	v_pk_mul_f32 v[10:11], v[4:5], v[156:157] op_sel:[0,1]
	v_pk_mul_f32 v[4:5], v[2:3], v[156:157] op_sel:[0,1]
	v_cvt_pk_bf16_f32 v2, v6, v7
	v_cvt_pk_bf16_f32 v3, v8, v9
	s_nop 0
	v_cvt_pk_bf16_f32 v4, v4, v5
	v_cvt_pk_bf16_f32 v5, v10, v11
	global_store_dwordx4 v[18:19], v[2:5], off offset:256
	s_cbranch_vccnz .LBB0_1166
	s_andn2_b64 vcc, exec, s[20:21]
	s_cbranch_vccnz .LBB0_1165
	s_barrier
	s_branch .LBB0_1165
